# speedup vs baseline: 1.0241x; 1.0241x over previous
_Z11prep_kernelPKfS0_S0_S0_S0_PDF16_S1_S1_P15HIP_vector_typeIfLj2EE:
	s_load_dwordx8 s[4:11], s[0:1], 0x28
	s_load_dwordx8 s[16:23], s[0:1], 0x0
	s_load_dwordx2 s[24:25], s[0:1], 0x20
	s_mov_b32 s3, 0xfffffe00
	s_cmpk_lt_u32 s2, 0x200
	s_cselect_b32 s3, 0x1000, s3
	s_add_i32 s2, s2, s3
	s_cmpk_gt_i32 s2, 0x7ff
	s_mov_b64 s[12:13], -1
	s_cbranch_scc1 .LBB0_3
	s_andn2_b64 vcc, exec, s[12:13]
	s_cbranch_vccz .LBB0_12

.LBB0_6:
	s_andn2_b64 vcc, exec, s[12:13]
	s_cbranch_vccnz .LBB0_8
	s_waitcnt lgkmcnt(0)
	s_mov_b64 s[10:11], s[24:25]
	s_add_i32 s12, s2, 0xfffff200
	s_mov_b32 s13, 0
	s_lshl_b64 s[12:13], s[12:13], 11
	v_lshl_or_b32 v10, v0, 3, s12
	v_mov_b32_e32 v11, s13
	s_waitcnt lgkmcnt(0)
	v_lshl_add_u64 v[12:13], v[10:11], 2, s[10:11]
	global_load_dwordx4 v[2:5], v[12:13], off offset:16 nt
	global_load_dwordx4 v[6:9], v[12:13], off nt
	v_mov_b32_e32 v12, s8
	v_mov_b32_e32 v13, s9
	s_movk_i32 s3, 0x880
	v_lshlrev_b32_e32 v11, 4, v0
	v_alignbit_b32 v10, s13, v10, 10
	v_mov_b32_e32 v1, 0x880
	v_and_b32_e32 v14, 0x7f0, v11
	s_lshr_b32 s10, s13, 10
	v_mad_u64_u32 v[10:11], s[8:9], v10, s3, v[12:13]
	v_mov_b32_e32 v15, 0
	v_mad_u32_u24 v11, s10, v1, v11
	v_lshl_add_u64 v[10:11], v[10:11], 0, v[14:15]
	s_waitcnt vmcnt(1)
	v_cvt_pk_f16_f32 v5, v4, v5
	v_cvt_pk_f16_f32 v4, v2, v3
	s_waitcnt vmcnt(0)
	v_cvt_pk_f16_f32 v3, v8, v9
	v_cvt_pk_f16_f32 v2, v6, v7
	global_store_dwordx4 v[10:11], v[2:5], off sc1
	s_nop 1

.LBB0_9:
	s_andn2_b64 vcc, exec, s[12:13]
	s_cbranch_vccnz .LBB0_11
	s_add_i32 s14, s2, 0xfffff800
	s_mov_b32 s15, 0
	s_lshl_b64 s[14:15], s[14:15], 11
	v_lshlrev_b32_e32 v1, 3, v0
	v_or_b32_e32 v2, s14, v1
	v_alignbit_b32 v14, s15, v2, 10
	v_mul_u32_u24_e32 v3, 0xaaab, v14
	v_lshrrev_b32_e32 v3, 23, v3
	v_lshrrev_b32_e32 v2, 10, v2
	v_mul_lo_u16_e32 v3, 0xc0, v3
	v_sub_u16_e32 v2, v2, v3
	s_movk_i32 s14, 0x60
	s_movk_i32 s3, 0x5f
	v_add_u32_e32 v3, 0xffffffa0, v2
	v_cmp_gt_u16_e32 vcc, s14, v2
	s_waitcnt lgkmcnt(0)
	s_mov_b64 s[8:9], s[18:19]
	s_mov_b64 s[10:11], s[20:21]
	s_mov_b64 s[12:13], s[22:23]
	v_cndmask_b32_e32 v3, v3, v2, vcc
	v_cmp_lt_u16_e32 vcc, s3, v2
	v_lshrrev_b32_e32 v5, 5, v3
	v_lshlrev_b32_e32 v3, 1, v3
	v_cndmask_b32_e64 v6, 0, 3, vcc
	v_add_u32_e32 v5, v5, v6
	v_and_b32_e32 v4, 15, v2
	v_sub_u32_e32 v2, v14, v2
	v_lshlrev_b32_e32 v6, 5, v5
	v_and_b32_e32 v3, 32, v3
	v_lshlrev_b32_e32 v5, 4, v5
	v_and_b32_e32 v6, 0x3c0, v6
	v_and_b32_e32 v5, 16, v5
	v_add3_u32 v2, v2, v4, v3
	v_add3_u32 v4, v2, v6, v5
	s_movk_i32 s3, 0x400
	v_and_b32_e32 v2, 0xc00, v4
	s_waitcnt lgkmcnt(0)
	v_mov_b32_e32 v3, s12
	v_mov_b32_e32 v5, s10
	v_cmp_eq_u32_e32 vcc, s3, v2
	v_and_b32_e32 v1, 0x3f8, v1
	v_mov_b32_e32 v11, 0
	v_cndmask_b32_e32 v2, v3, v5, vcc
	v_mov_b32_e32 v3, s13
	v_mov_b32_e32 v5, s11
	v_cndmask_b32_e32 v3, v3, v5, vcc
	v_mov_b32_e32 v5, s9
	v_cmp_gt_u32_e32 vcc, s3, v4
	v_lshlrev_b32_e32 v4, 12, v4
	v_and_b32_e32 v10, 0x3ff000, v4
	v_cndmask_b32_e32 v3, v3, v5, vcc
	v_mov_b32_e32 v5, s8
	v_cndmask_b32_e32 v2, v2, v5, vcc
	v_lshl_add_u64 v[2:3], v[2:3], 0, v[10:11]
	v_lshlrev_b32_e32 v10, 2, v1
	v_lshl_add_u64 v[12:13], v[2:3], 0, v[10:11]
	global_load_dwordx4 v[2:5], v[12:13], off offset:16 nt
	global_load_dwordx4 v[6:9], v[12:13], off nt
	v_mov_b32_e32 v12, s6
	v_mov_b32_e32 v13, s7
	s_movk_i32 s3, 0x880
	v_mov_b32_e32 v10, 0x880
	s_lshr_b32 s8, s15, 10
	v_mad_u64_u32 v[12:13], s[6:7], v14, s3, v[12:13]
	v_mad_u32_u24 v13, s8, v10, v13
	v_lshlrev_b32_e32 v10, 1, v1
	v_lshl_add_u64 v[10:11], v[12:13], 0, v[10:11]
	s_waitcnt vmcnt(1)
	v_cvt_pk_f16_f32 v5, v4, v5
	v_cvt_pk_f16_f32 v4, v2, v3
	s_waitcnt vmcnt(0)
	v_cvt_pk_f16_f32 v3, v8, v9
	v_cvt_pk_f16_f32 v2, v6, v7
	global_store_dwordx4 v[10:11], v[2:5], off sc1
	s_nop 1

.LBB0_12:
	s_ashr_i32 s3, s2, 31
	s_waitcnt lgkmcnt(0)
	s_mov_b64 s[0:1], s[16:17]
	s_lshl_b64 s[6:7], s[2:3], 11
	v_lshl_or_b32 v8, v0, 3, s6
	v_mov_b32_e32 v9, s7
	v_lshl_add_u64 v[10:11], v[8:9], 2, s[0:1]
	global_load_dwordx4 v[0:3], v[10:11], off offset:16 nt
	global_load_dwordx4 v[4:7], v[10:11], off nt
	s_mov_b32 s1, 0
	s_lshr_b32 s0, s3, 22
	v_lshl_add_u64 v[12:13], v[8:9], 0, s[0:1]
	v_mov_b32_e32 v10, s4
	v_mov_b32_e32 v11, s5
	s_movk_i32 s2, 0x880
	v_ashrrev_i64 v[14:15], 10, v[12:13]
	v_and_b32_e32 v12, 0xfffffc00, v12
	v_and_b32_e32 v13, 0x7fffffff, v13
	v_mad_u64_u32 v[10:11], s[0:1], v14, s2, v[10:11]
	v_sub_co_u32_e32 v8, vcc, v8, v12
	v_mad_i32_i24 v11, v15, s2, v11
	s_nop 0
	v_subb_co_u32_e32 v9, vcc, v9, v13, vcc
	v_lshl_add_u64 v[8:9], v[8:9], 1, v[10:11]
	s_waitcnt vmcnt(1)
	v_cvt_pk_f16_f32 v3, v2, v3
	v_cvt_pk_f16_f32 v2, v0, v1
	s_waitcnt vmcnt(0)
	v_cvt_pk_f16_f32 v1, v6, v7
	v_cvt_pk_f16_f32 v0, v4, v5
	global_store_dwordx4 v[8:9], v[0:3], off sc1
	s_nop 1
	s_endpgm

	.amdhsa_kernel _Z11prep_kernelPKfS0_S0_S0_S0_PDF16_S1_S1_P15HIP_vector_typeIfLj2EE
		.amdhsa_group_segment_fixed_size 0
		.amdhsa_private_segment_fixed_size 0
		.amdhsa_kernarg_size 72
		.amdhsa_user_sgpr_count 2
		.amdhsa_user_sgpr_dispatch_ptr 0
		.amdhsa_user_sgpr_queue_ptr 0
		.amdhsa_user_sgpr_kernarg_segment_ptr 1
		.amdhsa_user_sgpr_dispatch_id 0
		.amdhsa_user_sgpr_kernarg_preload_length 0
		.amdhsa_user_sgpr_kernarg_preload_offset 0
		.amdhsa_user_sgpr_private_segment_size 0
		.amdhsa_uses_dynamic_stack 0
		.amdhsa_enable_private_segment 0
		.amdhsa_system_sgpr_workgroup_id_x 1
		.amdhsa_system_sgpr_workgroup_id_y 0
		.amdhsa_system_sgpr_workgroup_id_z 0
		.amdhsa_system_sgpr_workgroup_info 0
		.amdhsa_system_vgpr_workitem_id 0
		.amdhsa_next_free_vgpr 20
		.amdhsa_next_free_sgpr 26
		.amdhsa_accum_offset 20
		.amdhsa_reserve_vcc 1
		.amdhsa_float_round_mode_32 0
		.amdhsa_float_round_mode_16_64 0
		.amdhsa_float_denorm_mode_32 3
		.amdhsa_float_denorm_mode_16_64 3
		.amdhsa_dx10_clamp 1
		.amdhsa_ieee_mode 1
		.amdhsa_fp16_overflow 0
		.amdhsa_tg_split 0
		.amdhsa_exception_fp_ieee_invalid_op 0
		.amdhsa_exception_fp_denorm_src 0
		.amdhsa_exception_fp_ieee_div_zero 0
		.amdhsa_exception_fp_ieee_overflow 0
		.amdhsa_exception_fp_ieee_underflow 0
		.amdhsa_exception_fp_ieee_inexact 0
		.amdhsa_exception_int_div_zero 0
	.end_amdhsa_kernel

amdhsa.kernels:
  - .agpr_count:     0
    .args:
      - .actual_access:  read_only
        .address_space:  global
        .offset:         0
        .size:           8
        .value_kind:     global_buffer
      - .actual_access:  read_only
        .address_space:  global
        .offset:         8
        .size:           8
        .value_kind:     global_buffer
      - .actual_access:  read_only
        .address_space:  global
        .offset:         16
        .size:           8
        .value_kind:     global_buffer
      - .actual_access:  read_only
        .address_space:  global
        .offset:         24
        .size:           8
        .value_kind:     global_buffer
      - .actual_access:  read_only
        .address_space:  global
        .offset:         32
        .size:           8
        .value_kind:     global_buffer
      - .address_space:  global
        .offset:         40
        .size:           8
        .value_kind:     global_buffer
      - .address_space:  global
        .offset:         48
        .size:           8
        .value_kind:     global_buffer
      - .address_space:  global
        .offset:         56
        .size:           8
        .value_kind:     global_buffer
      - .address_space:  global
        .offset:         64
        .size:           8
        .value_kind:     global_buffer
    .group_segment_fixed_size: 0
    .kernarg_segment_align: 8
    .kernarg_segment_size: 72
    .language:       OpenCL C
    .language_version:
      - 2
      - 0
    .max_flat_workgroup_size: 256
    .name:           _Z11prep_kernelPKfS0_S0_S0_S0_PDF16_S1_S1_P15HIP_vector_typeIfLj2EE
    .private_segment_fixed_size: 0
    .sgpr_count:     32
    .sgpr_spill_count: 0
    .symbol:         _Z11prep_kernelPKfS0_S0_S0_S0_PDF16_S1_S1_P15HIP_vector_typeIfLj2EE.kd
    .uniform_work_group_size: 1
    .uses_dynamic_stack: false
    .vgpr_count:     20
    .vgpr_spill_count: 0
    .wavefront_size: 64
  - .agpr_count:     0
    .args:
      - .address_space:  global
        .offset:         0
        .size:           8
        .value_kind:     global_buffer
      - .address_space:  global
        .offset:         8
        .size:           8
        .value_kind:     global_buffer
      - .address_space:  global
        .offset:         16
        .size:           8
        .value_kind:     global_buffer
      - .address_space:  global
        .offset:         24
        .size:           8
        .value_kind:     global_buffer
    .group_segment_fixed_size: 0
    .kernarg_segment_align: 8
    .kernarg_segment_size: 32
    .language:       OpenCL C
    .language_version:
      - 2
      - 0
    .max_flat_workgroup_size: 512
    .name:           _Z10attn64_fwdPKDF16_S0_S0_PDF16_
    .private_segment_fixed_size: 0
    .sgpr_count:     48
    .sgpr_spill_count: 0
    .symbol:         _Z10attn64_fwdPKDF16_S0_S0_PDF16_.kd
    .uniform_work_group_size: 1
    .uses_dynamic_stack: false
    .vgpr_count:     252
    .vgpr_spill_count: 0
    .wavefront_size: 64
  - .agpr_count:     0
    .args:
      - .address_space:  global
        .offset:         0
        .size:           8
        .value_kind:     global_buffer
      - .address_space:  global
        .offset:         8
        .size:           8
        .value_kind:     global_buffer
      - .address_space:  global
        .offset:         16
        .size:           8
        .value_kind:     global_buffer
      - .address_space:  global
        .offset:         24
        .size:           8
        .value_kind:     global_buffer
      - .address_space:  global
        .offset:         32
        .size:           8
        .value_kind:     global_buffer
      - .address_space:  global
        .offset:         40
        .size:           8
        .value_kind:     global_buffer
      - .actual_access:  read_only
        .address_space:  global
        .offset:         48
        .size:           8
        .value_kind:     global_buffer
      - .offset:         56
        .size:           4
        .value_kind:     by_value
      - .offset:         60
        .size:           4
        .value_kind:     by_value
      - .offset:         64
        .size:           4
        .value_kind:     by_value
    .group_segment_fixed_size: 32768
    .kernarg_segment_align: 8
    .kernarg_segment_size: 68
    .language:       OpenCL C
    .language_version:
      - 2
      - 0
    .max_flat_workgroup_size: 768
    .name:           _Z7gemm_dbILi256ELi192ELi64ELi96ELi64ELi2ELi1ELi4EEvPKDF16_S1_PfPDF16_S3_S3_PK15HIP_vector_typeIfLj2EEiii
    .private_segment_fixed_size: 0
    .sgpr_count:     27
    .sgpr_spill_count: 0
    .symbol:         _Z7gemm_dbILi256ELi192ELi64ELi96ELi64ELi2ELi1ELi4EEvPKDF16_S1_PfPDF16_S3_S3_PK15HIP_vector_typeIfLj2EEiii.kd
    .uniform_work_group_size: 1
    .uses_dynamic_stack: false
    .vgpr_count:     141
    .vgpr_spill_count: 0
    .wavefront_size: 64
  - .agpr_count:     0
    .args:
      - .address_space:  global
        .offset:         0
        .size:           8
        .value_kind:     global_buffer
      - .address_space:  global
        .offset:         8
        .size:           8
        .value_kind:     global_buffer
      - .address_space:  global
        .offset:         16
        .size:           8
        .value_kind:     global_buffer
      - .address_space:  global
        .offset:         24
        .size:           8
        .value_kind:     global_buffer
      - .address_space:  global
        .offset:         32
        .size:           8
        .value_kind:     global_buffer
      - .address_space:  global
        .offset:         40
        .size:           8
        .value_kind:     global_buffer
      - .actual_access:  read_only
        .address_space:  global
        .offset:         48
        .size:           8
        .value_kind:     global_buffer
      - .offset:         56
        .size:           4
        .value_kind:     by_value
      - .offset:         60
        .size:           4
        .value_kind:     by_value
      - .offset:         64
        .size:           4
        .value_kind:     by_value
    .group_segment_fixed_size: 0
    .kernarg_segment_align: 8
    .kernarg_segment_size: 68
    .language:       OpenCL C
    .language_version:
      - 2
      - 0
    .max_flat_workgroup_size: 512
    .name:           _Z7gemm_dbILi128ELi128ELi64ELi64ELi64ELi3ELi0ELi4EEvPKDF16_S1_PfPDF16_S3_S3_PK15HIP_vector_typeIfLj2EEiii
    .private_segment_fixed_size: 0
    .sgpr_count:     26
    .sgpr_spill_count: 0
    .symbol:         _Z7gemm_dbILi128ELi128ELi64ELi64ELi64ELi3ELi0ELi4EEvPKDF16_S1_PfPDF16_S3_S3_PK15HIP_vector_typeIfLj2EEiii.kd
    .uniform_work_group_size: 1
    .uses_dynamic_stack: false
    .vgpr_count:     168
    .vgpr_spill_count: 0
    .wavefront_size: 64
